# v21
# baseline (speedup 1.0000x reference)
_Z12pool1_kernelPKfS0_S0_S0_S0_S0_S0_S0_S0_S0_PfS1_:
	s_load_dwordx4 s[12:15], s[0:1], 0x0
	s_load_dwordx2 s[36:37], s[0:1], 0x48
	s_load_dwordx2 s[38:39], s[0:1], 0x58
	s_load_dwordx4 s[44:47], s[0:1], 0x10
	s_cmp_eq_u32 s2, 0
	s_movk_i32 s3, 0x80
	s_cselect_b64 s[4:5], -1, 0
	v_cmp_gt_u32_e64 s[10:11], s3, v0
	s_and_b64 s[6:7], s[4:5], s[10:11]
	s_and_saveexec_b64 s[4:5], s[6:7]
	s_cbranch_execz .LBB0_2
	v_mov_b32_e32 v1, 0
	v_lshlrev_b64 v[2:3], 2, v[0:1]
	s_waitcnt lgkmcnt(0)
	v_lshl_add_u64 v[4:5], s[36:37], 0, v[2:3]
	global_load_dword v253, v[4:5], off
	v_lshl_add_u64 v[254:255], s[38:39], 0, v[2:3]
.LBB0_2:
	s_or_b64 exec, exec, s[4:5]
	v_mov_b32_e32 v3, 0
	v_lshlrev_b32_e32 v130, 2, v0
	v_and_b32_e32 v131, 63, v0
	v_readfirstlane_b32 s3, v0
	v_lshlrev_b32_e32 v204, 4, v131
	v_lshlrev_b32_e32 v222, 4, v0
	v_add_u32_e32 v223, 0x2000, v222
	v_add_u32_e32 v224, 0x4000, v222
	v_add_u32_e32 v225, 0x6000, v222
	v_add_u32_e32 v226, 0x8000, v222
	v_add_u32_e32 v227, 0xa000, v222
	v_add_u32_e32 v228, 0xc000, v222
	v_add_u32_e32 v229, 0xe000, v222
	v_add_u32_e32 v230, 0x10000, v222
	v_add_u32_e32 v231, 0x12000, v222
	v_add_u32_e32 v232, 0x14000, v222
	v_add_u32_e32 v233, 0x16000, v222
	v_add_u32_e32 v234, 0x18000, v222
	v_add_u32_e32 v235, 0x1a000, v222
	v_add_u32_e32 v236, 0x1c000, v222
	v_add_u32_e32 v237, 0x1e000, v222
	s_lshr_b32 s31, s3, 6
	s_lshl_b32 s33, s2, 21
	s_mul_i32 s42, s31, 0x2200
	s_add_i32 s42, s42, 0x11000
	v_lshl_add_u32 v212, v131, 3, s42
	v_add_u32_e32 v215, 0x800, v212
	v_add_u32_e32 v216, 0x1000, v212
	v_add_u32_e32 v217, 0x1800, v212
	v_and_b32_e32 v250, 0x7f, v0
	v_lshlrev_b32_e32 v250, 2, v250
	s_lshl_b32 s6, s31, 14
	s_add_i32 s6, s6, s33
	s_waitcnt lgkmcnt(0)
	s_mov_b64 s[40:41], s[14:15]
	s_mov_b32 s15, 0x20000
	s_brev_b32 s14, -2
	s_and_b32 s13, s13, 0xffff
	s_or_b32 s7, s6, 0x1000
	buffer_load_dwordx4 v[34:37], v204, s[12:15], s6 offen sc0 nt sc1
	buffer_load_dwordx4 v[38:41], v204, s[12:15], s7 offen sc0 nt sc1
	s_or_b32 s7, s6, 0x2000
	s_or_b32 s8, s6, 0x3000
	buffer_load_dwordx4 v[42:45], v204, s[12:15], s7 offen sc0 nt sc1
	buffer_load_dwordx4 v[46:49], v204, s[12:15], s8 offen sc0 nt sc1
	s_or_b32 s7, s6, 0x400
	s_or_b32 s8, s6, 0x1400
	buffer_load_dwordx4 v[50:53], v204, s[12:15], s7 offen sc0 nt sc1
	buffer_load_dwordx4 v[54:57], v204, s[12:15], s8 offen sc0 nt sc1
	s_or_b32 s7, s6, 0x2400
	s_or_b32 s8, s6, 0x3400
	buffer_load_dwordx4 v[58:61], v204, s[12:15], s7 offen sc0 nt sc1
	buffer_load_dwordx4 v[62:65], v204, s[12:15], s8 offen sc0 nt sc1
	s_or_b32 s7, s6, 0x800
	s_or_b32 s8, s6, 0x1800
	buffer_load_dwordx4 v[66:69], v204, s[12:15], s7 offen sc0 nt sc1
	buffer_load_dwordx4 v[70:73], v204, s[12:15], s8 offen sc0 nt sc1
	s_or_b32 s7, s6, 0x2800
	s_or_b32 s8, s6, 0x3800
	buffer_load_dwordx4 v[74:77], v204, s[12:15], s7 offen sc0 nt sc1
	buffer_load_dwordx4 v[78:81], v204, s[12:15], s8 offen sc0 nt sc1
	s_or_b32 s7, s6, 0xc00
	s_or_b32 s8, s6, 0x1c00
	buffer_load_dwordx4 v[82:85], v204, s[12:15], s7 offen sc0 nt sc1
	buffer_load_dwordx4 v[86:89], v204, s[12:15], s8 offen sc0 nt sc1
	s_or_b32 s7, s6, 0x2c00
	s_or_b32 s6, s6, 0x3c00
	buffer_load_dwordx4 v[90:93], v204, s[12:15], s7 offen sc0 nt sc1
	buffer_load_dwordx4 v[94:97], v204, s[12:15], s6 offen sc0 nt sc1
	global_load_dwordx4 v[4:7], v222, s[40:41]
	global_load_dwordx4 v[8:11], v223, s[40:41]
	global_load_dwordx4 v[12:15], v224, s[40:41]
	global_load_dwordx4 v[16:19], v225, s[40:41]
	global_load_dwordx4 v[20:23], v226, s[40:41]
	global_load_dwordx4 v[24:27], v227, s[40:41]
	global_load_dwordx4 v[28:31], v228, s[40:41]
	global_load_dwordx4 v[98:101], v229, s[40:41]
	global_load_dwordx4 v[102:105], v230, s[40:41]
	global_load_dwordx4 v[106:109], v231, s[40:41]
	global_load_dwordx4 v[110:113], v232, s[40:41]
	global_load_dwordx4 v[114:117], v233, s[40:41]
	global_load_dwordx4 v[118:121], v234, s[40:41]
	global_load_dwordx4 v[122:125], v235, s[40:41]
	global_load_dwordx4 v[126:129], v236, s[40:41]
	global_load_dwordx4 v[132:135], v237, s[40:41]
	global_load_dword v248, v250, s[44:45]
	global_load_dword v249, v250, s[46:47]
	s_load_dwordx2 s[20:21], s[0:1], 0x50
	s_load_dwordx2 s[22:23], s[0:1], 0x40
	s_load_dwordx2 s[4:5], s[0:1], 0x20
	s_load_dwordx4 s[16:19], s[0:1], 0x30
	s_waitcnt vmcnt(33)
	v_cvt_pk_bf16_f32 v238, v34, v35
	v_cvt_pk_bf16_f32 v239, v36, v37
	s_waitcnt vmcnt(29)
	v_cvt_pk_bf16_f32 v246, v50, v51
	v_cvt_pk_bf16_f32 v247, v52, v53
	v_cvt_pk_bf16_f32 v240, v38, v39
	v_cvt_pk_bf16_f32 v241, v40, v41
	ds_write2_b64 v212, v[238:239], v[246:247] offset1:68
	s_waitcnt vmcnt(28)
	v_cvt_pk_bf16_f32 v238, v54, v55
	v_cvt_pk_bf16_f32 v239, v56, v57
	v_cvt_pk_bf16_f32 v242, v42, v43
	v_cvt_pk_bf16_f32 v243, v44, v45
	ds_write2_b64 v215, v[240:241], v[238:239] offset0:16 offset1:84
	s_waitcnt vmcnt(27)
	v_cvt_pk_bf16_f32 v238, v58, v59
	v_cvt_pk_bf16_f32 v239, v60, v61
	v_cvt_pk_bf16_f32 v244, v46, v47
	v_cvt_pk_bf16_f32 v245, v48, v49
	ds_write2_b64 v216, v[242:243], v[238:239] offset0:32 offset1:100
	s_waitcnt vmcnt(26)
	v_cvt_pk_bf16_f32 v238, v62, v63
	v_cvt_pk_bf16_f32 v239, v64, v65
	ds_write2_b64 v217, v[244:245], v[238:239] offset0:48 offset1:116
	s_waitcnt vmcnt(25)
	v_cvt_pk_bf16_f32 v238, v66, v67
	v_cvt_pk_bf16_f32 v239, v68, v69
	s_waitcnt vmcnt(21)
	v_cvt_pk_bf16_f32 v246, v82, v83
	v_cvt_pk_bf16_f32 v247, v84, v85
	v_cvt_pk_bf16_f32 v240, v70, v71
	v_cvt_pk_bf16_f32 v241, v72, v73
	ds_write2_b64 v212, v[238:239], v[246:247] offset0:136 offset1:204
	s_waitcnt vmcnt(20)
	v_cvt_pk_bf16_f32 v238, v86, v87
	v_cvt_pk_bf16_f32 v239, v88, v89
	v_cvt_pk_bf16_f32 v242, v74, v75
	v_cvt_pk_bf16_f32 v243, v76, v77
	ds_write2_b64 v215, v[240:241], v[238:239] offset0:152 offset1:220
	s_waitcnt vmcnt(19)
	v_cvt_pk_bf16_f32 v238, v90, v91
	v_cvt_pk_bf16_f32 v239, v92, v93
	v_cvt_pk_bf16_f32 v244, v78, v79
	v_cvt_pk_bf16_f32 v245, v80, v81
	ds_write2_b64 v216, v[242:243], v[238:239] offset0:168 offset1:236
	s_waitcnt vmcnt(18)
	v_cvt_pk_bf16_f32 v238, v94, v95
	v_cvt_pk_bf16_f32 v239, v96, v97
	ds_write2_b64 v217, v[244:245], v[238:239] offset0:184 offset1:252
	s_add_i32 s26, s31, 8
	s_lshl_b32 s24, s26, 14
	s_add_i32 s24, s24, s33
	s_or_b32 s25, s24, 0x1000
	buffer_load_dwordx4 v[34:37], v204, s[12:15], s24 offen sc0 nt sc1
	buffer_load_dwordx4 v[38:41], v204, s[12:15], s25 offen sc0 nt sc1
	s_or_b32 s25, s24, 0x2000
	s_or_b32 s27, s24, 0x3000
	buffer_load_dwordx4 v[42:45], v204, s[12:15], s25 offen sc0 nt sc1
	buffer_load_dwordx4 v[46:49], v204, s[12:15], s27 offen sc0 nt sc1
	s_or_b32 s25, s24, 0x400
	s_or_b32 s27, s24, 0x1400
	buffer_load_dwordx4 v[50:53], v204, s[12:15], s25 offen sc0 nt sc1
	buffer_load_dwordx4 v[54:57], v204, s[12:15], s27 offen sc0 nt sc1
	s_or_b32 s25, s24, 0x2400
	s_or_b32 s27, s24, 0x3400
	buffer_load_dwordx4 v[58:61], v204, s[12:15], s25 offen sc0 nt sc1
	buffer_load_dwordx4 v[62:65], v204, s[12:15], s27 offen sc0 nt sc1
	s_or_b32 s25, s24, 0x800
	s_or_b32 s27, s24, 0x1800
	buffer_load_dwordx4 v[66:69], v204, s[12:15], s25 offen sc0 nt sc1
	buffer_load_dwordx4 v[70:73], v204, s[12:15], s27 offen sc0 nt sc1
	s_or_b32 s25, s24, 0x2800
	s_or_b32 s27, s24, 0x3800
	buffer_load_dwordx4 v[74:77], v204, s[12:15], s25 offen sc0 nt sc1
	buffer_load_dwordx4 v[78:81], v204, s[12:15], s27 offen sc0 nt sc1
	s_or_b32 s25, s24, 0xc00
	s_or_b32 s27, s24, 0x1c00
	buffer_load_dwordx4 v[82:85], v204, s[12:15], s25 offen sc0 nt sc1
	buffer_load_dwordx4 v[86:89], v204, s[12:15], s27 offen sc0 nt sc1
	s_or_b32 s25, s24, 0x2c00
	s_or_b32 s24, s24, 0x3c00
	buffer_load_dwordx4 v[90:93], v204, s[12:15], s25 offen sc0 nt sc1
	buffer_load_dwordx4 v[94:97], v204, s[12:15], s24 offen sc0 nt sc1
	v_lshlrev_b32_e32 v2, 3, v0
	v_and_b32_e32 v1, 0x1f8, v2
	v_lshrrev_b32_e32 v32, 6, v0
	s_movk_i32 s6, 0x220
	s_waitcnt vmcnt(16)
	v_cvt_pk_bf16_f32 v4, v4, v5
	v_cvt_pk_bf16_f32 v5, v6, v7
	v_mad_u32_u24 v6, v32, s6, v1
	ds_write_b64 v6, v[4:5]
	v_add_u32_e32 v4, 0x200, v0
	v_lshrrev_b32_e32 v7, 6, v4
	s_waitcnt vmcnt(16)
	v_cvt_pk_bf16_f32 v4, v8, v9
	v_cvt_pk_bf16_f32 v5, v10, v11
	v_mad_u32_u24 v7, v7, s6, v1
	ds_write_b64 v7, v[4:5]
	s_waitcnt vmcnt(16)
	v_cvt_pk_bf16_f32 v4, v12, v13
	v_cvt_pk_bf16_f32 v5, v14, v15
	ds_write_b64 v6, v[4:5] offset:8704
	v_add_u32_e32 v4, 0x600, v0
	v_lshrrev_b32_e32 v7, 6, v4
	s_waitcnt vmcnt(16)
	v_cvt_pk_bf16_f32 v4, v16, v17
	v_cvt_pk_bf16_f32 v5, v18, v19
	v_mad_u32_u24 v7, v7, s6, v1
	ds_write_b64 v7, v[4:5]
	s_waitcnt vmcnt(16)
	v_cvt_pk_bf16_f32 v4, v20, v21
	v_cvt_pk_bf16_f32 v5, v22, v23
	ds_write_b64 v6, v[4:5] offset:17408
	v_add_u32_e32 v4, 0xa00, v0
	v_lshrrev_b32_e32 v7, 6, v4
	s_waitcnt vmcnt(16)
	v_cvt_pk_bf16_f32 v4, v24, v25
	v_cvt_pk_bf16_f32 v5, v26, v27
	v_mad_u32_u24 v7, v7, s6, v1
	ds_write_b64 v7, v[4:5]
	s_waitcnt vmcnt(16)
	v_cvt_pk_bf16_f32 v4, v28, v29
	v_cvt_pk_bf16_f32 v5, v30, v31
	ds_write_b64 v6, v[4:5] offset:26112
	v_add_u32_e32 v4, 0xe00, v0
	v_lshrrev_b32_e32 v7, 6, v4
	s_waitcnt vmcnt(16)
	v_cvt_pk_bf16_f32 v4, v98, v99
	v_cvt_pk_bf16_f32 v5, v100, v101
	v_mad_u32_u24 v7, v7, s6, v1
	ds_write_b64 v7, v[4:5]
	s_waitcnt vmcnt(16)
	v_cvt_pk_bf16_f32 v4, v102, v103
	v_cvt_pk_bf16_f32 v5, v104, v105
	ds_write_b64 v6, v[4:5] offset:34816
	v_add_u32_e32 v4, 0x1200, v0
	v_lshrrev_b32_e32 v7, 6, v4
	s_waitcnt vmcnt(16)
	v_cvt_pk_bf16_f32 v4, v106, v107
	v_cvt_pk_bf16_f32 v5, v108, v109
	v_mad_u32_u24 v7, v7, s6, v1
	ds_write_b64 v7, v[4:5]
	s_waitcnt vmcnt(16)
	v_cvt_pk_bf16_f32 v4, v110, v111
	v_cvt_pk_bf16_f32 v5, v112, v113
	ds_write_b64 v6, v[4:5] offset:43520
	v_add_u32_e32 v4, 0x1600, v0
	v_lshrrev_b32_e32 v7, 6, v4
	s_waitcnt vmcnt(16)
	v_cvt_pk_bf16_f32 v4, v114, v115
	v_cvt_pk_bf16_f32 v5, v116, v117
	v_mad_u32_u24 v7, v7, s6, v1
	ds_write_b64 v7, v[4:5]
	s_waitcnt vmcnt(16)
	v_cvt_pk_bf16_f32 v4, v118, v119
	v_cvt_pk_bf16_f32 v5, v120, v121
	ds_write_b64 v6, v[4:5] offset:52224
	v_add_u32_e32 v4, 0x1a00, v0
	v_lshrrev_b32_e32 v7, 6, v4
	s_waitcnt vmcnt(16)
	v_cvt_pk_bf16_f32 v4, v122, v123
	v_cvt_pk_bf16_f32 v5, v124, v125
	v_mad_u32_u24 v7, v7, s6, v1
	ds_write_b64 v7, v[4:5]
	s_waitcnt vmcnt(16)
	v_cvt_pk_bf16_f32 v4, v126, v127
	v_cvt_pk_bf16_f32 v5, v128, v129
	ds_write_b64 v6, v[4:5] offset:60928
	v_add_u32_e32 v4, 0x1e00, v0
	v_lshrrev_b32_e32 v6, 6, v4
	s_waitcnt vmcnt(16)
	v_cvt_pk_bf16_f32 v4, v132, v133
	v_cvt_pk_bf16_f32 v5, v134, v135
	v_mad_u32_u24 v1, v6, s6, v1
	ds_write_b64 v1, v[4:5]
	s_and_saveexec_b64 s[6:7], s[10:11]
	s_cbranch_execz .LBB0_4
	v_add_u32_e32 v5, 0x22000, v130
	v_add_u32_e32 v6, 0x22200, v130
	v_mul_f32_e32 v1, 0x4038aa3b, v248
	ds_write_b32 v5, v1
	ds_write_b32 v6, v249

.Lp1_noinit:
	s_or_b64 exec, exec, s[26:27]
	s_add_i32 s26, s31, 8
	s_branch .LBB0_17
